# speedup vs baseline: 1.0340x; 1.0340x over previous
_Z11gram_kernelPKfPKiS0_S0_S0_S0_S0_S0_S0_S0_S0_Pf:
	s_load_dwordx4 s[24:27], s[0:1], 0x0
	s_load_dwordx2 s[28:29], s[0:1], 0x40
	s_load_dwordx4 s[20:23], s[0:1], 0x30
	s_load_dwordx2 s[10:11], s[0:1], 0x58
	s_load_dwordx2 s[44:45], s[0:1], 0x20
	s_load_dwordx2 s[68:69], s[0:1], 0x10
	s_load_dwordx2 s[60:61], s[0:1], 0x18
	s_load_dwordx2 s[62:63], s[0:1], 0x28
	s_load_dwordx2 s[64:65], s[0:1], 0x48
	s_load_dwordx2 s[66:67], s[0:1], 0x50
	s_ashr_i32 s30, s2, 1
	v_mov_b32_e32 v11, 0
	s_ashr_i32 s31, s30, 31
	s_lshl_b32 s46, s30, 11
	s_lshl_b32 s3, s2, 10
	s_ashr_i32 s47, s46, 31
	s_and_b32 s33, s3, 0x400
	v_lshlrev_b32_e32 v46, 2, v0
	v_mov_b32_e32 v47, 0
	v_lshlrev_b32_e32 v212, 1, v0
	v_mov_b32_e32 v213, v47
	v_lshrrev_b32_e32 v219, 6, v0
	v_bfe_u32 v214, v0, 5, 1
	v_and_b32_e32 v220, 31, v0
	s_or_b32 s3, s46, s33
	v_lshlrev_b32_e32 v216, 4, v219
	v_lshlrev_b32_e32 v221, 3, v214
	v_or3_b32 v1, s3, v216, v221
	v_lshlrev_b32_e32 v232, 4, v220
	v_and_b32_e32 v218, 63, v0
	s_mov_b32 s39, 0x20000
	s_brev_b32 s38, 16
	v_lshl_or_b32 v180, v1, 9, v232
	v_add_u32_e32 v1, 0x10000, v180
	s_lshl_b64 s[4:5], s[46:47], 2
	s_lshl_b32 s3, s33, 2
	v_lshlrev_b32_e32 v251, 7, v0
	v_and_b32_e32 v252, 0x3fff, v251
	v_and_b32_e32 v253, 0x1fc, v46
	s_lshl_b64 s[6:7], s[30:31], 14
	s_waitcnt lgkmcnt(0)
	s_add_u32 s48, s20, s6
	s_addc_u32 s49, s21, s7
	s_mov_b64 s[36:37], s[24:25]
	s_and_b32 s37, s37, 0xffff
	s_add_u32 s26, s26, s4
	s_addc_u32 s27, s27, s5
	s_add_u32 s26, s26, s3
	s_addc_u32 s27, s27, 0
	v_lshl_add_u64 v[32:33], v[212:213], 2, s[26:27]
	global_load_dwordx2 v[32:33], v[32:33], off
	buffer_load_dwordx4 v[34:37], v180, s[36:39], 0 offen nt
	buffer_load_dwordx4 v[38:41], v180, s[36:39], 0 offen offset:512 nt
	buffer_load_dwordx4 v[42:45], v180, s[36:39], 0 offen offset:1024 nt
	buffer_load_dwordx4 v[96:99], v180, s[36:39], 0 offen offset:1536 nt
	buffer_load_dwordx4 v[100:103], v180, s[36:39], 0 offen offset:2048 nt
	buffer_load_dwordx4 v[104:107], v180, s[36:39], 0 offen offset:2560 nt
	buffer_load_dwordx4 v[108:111], v180, s[36:39], 0 offen offset:3072 nt
	buffer_load_dwordx4 v[112:115], v180, s[36:39], 0 offen offset:3584 nt
	global_load_dword v250, v47, s[22:23]
	global_load_dword v250, v47, s[28:29]
	global_load_dword v250, v47, s[68:69]
	global_load_dword v250, v47, s[44:45]
	global_load_dword v250, v47, s[48:49]
	global_load_dword v250, v47, s[60:61]
	global_load_dword v250, v47, s[62:63]
	global_load_dword v250, v47, s[64:65]
	global_load_dword v250, v47, s[66:67]
	buffer_load_dwordx4 v[116:119], v1, s[36:39], 0 offen nt
	buffer_load_dwordx4 v[120:123], v1, s[36:39], 0 offen offset:512 nt
	buffer_load_dwordx4 v[124:127], v1, s[36:39], 0 offen offset:1024 nt
	buffer_load_dwordx4 v[128:131], v1, s[36:39], 0 offen offset:1536 nt
	buffer_load_dwordx4 v[132:135], v1, s[36:39], 0 offen offset:2048 nt
	buffer_load_dwordx4 v[136:139], v1, s[36:39], 0 offen offset:2560 nt
	buffer_load_dwordx4 v[140:143], v1, s[36:39], 0 offen offset:3072 nt
	buffer_load_dwordx4 v[144:147], v1, s[36:39], 0 offen offset:3584 nt
	s_movk_i32 s3, 0x160
	v_cmp_gt_u32_e32 vcc, s3, v0
	s_mov_b32 s3, 0x10000
	v_lshrrev_b32_e32 v227, 5, v0
	v_and_b32_e32 v228, 0x7c, v46
	v_add_u32_e32 v2, 0x200, v0
	v_lshrrev_b32_e32 v229, 5, v2
	v_mul_u32_u24_e32 v246, 0x110, v227
	v_lshl_add_u32 v246, v220, 3, v246
	v_add_u32_e32 v246, 0x10000, v246
	v_lshlrev_b32_e32 v247, 2, v46
	s_waitcnt vmcnt(25)
	v_cmp_ne_u32_e64 s[6:7], 0, v32
	v_cmp_ne_u32_e64 s[4:5], 0, v33
	v_cmp_eq_u32_e64 s[8:9], 0, v218
	s_nop 0
	s_and_saveexec_b64 s[12:13], s[8:9]
	s_cbranch_execz .LBB0_6
	s_bcnt1_i32_b64 s6, s[6:7]
	s_bcnt1_i32_b64 s4, s[4:5]
	v_mov_b32_e32 v1, 0x21100
	s_add_i32 s4, s4, s6
	v_lshl_add_u32 v1, v219, 2, v1
	v_mov_b32_e32 v2, s4
	ds_write_b32 v1, v2
